# pass-2 mLSTM items: gate-scan/state loads of waves 0,1 consumed after the tile work instead of before (on top of v22)
# baseline (speedup 1.0000x reference)
.LBB0_979:
	s_and_b64 vcc, exec, s[0:1]
	s_cbranch_vccz .LBB0_814
	s_waitcnt vmcnt(4)
	v_mov_b32 v149, v0
	s_waitcnt vmcnt(1)
	v_ashrrev_i32_e32 v5, 6, v149
	v_and_b32_e32 v4, 63, v149
	v_cmp_gt_i32_e32 vcc, 2, v5
	s_barrier
	s_and_saveexec_b64 s[0:1], vcc
	s_cbranch_execz .LBB0_982
	s_lshl_b32 s9, s55, 4
	s_lshl_b32 s14, s38, 1
	s_or_b32 s9, s14, s9
	s_and_b64 s[14:15], s[66:67], exec
	s_waitcnt vmcnt(0)
	v_add_u32_e32 v6, s9, v5
	s_cselect_b32 s9, 0x41, 1
	s_sub_i32 s9, s9, s39
	s_add_i32 s30, s39, 2
	s_and_b64 s[14:15], s[66:67], exec
	s_cselect_b32 s14, s30, s42
	v_cmp_gt_u32_e32 vcc, 64, v149
	v_mov_b32_e32 v2, s9
	v_mov_b32_e32 v3, s14
	v_cndmask_b32_e32 v2, v2, v3, vcc
	v_ashrrev_i32_e32 v3, 31, v2
	s_movk_i32 s9, 0x42
	v_mad_i64_i32 v[2:3], s[14:15], v6, s9, v[2:3]
	s_load_dwordx2 s[14:15], s[76:77], 0x208
	s_load_dwordx4 s[40:43], s[76:77], 0x198
	v_xor_b32_e32 v6, 0x7f, v4
	v_cndmask_b32_e32 v16, v6, v4, vcc
	v_xor_b32_e32 v6, 63, v4
	v_or_b32_e32 v7, 64, v4
	v_cndmask_b32_e32 v17, v6, v7, vcc
	v_lshlrev_b64 v[6:7], 11, v[2:3]
	s_waitcnt lgkmcnt(0)
	v_lshl_add_u64 v[10:11], s[14:15], 0, v[6:7]
	v_lshlrev_b32_e32 v194, 4, v16
	v_lshl_add_u64 v[6:7], v[10:11], 0, v[194:195]
	v_lshlrev_b32_e32 v194, 4, v17
	v_mov_b32_e32 v14, s42
	v_mov_b32_e32 v15, s43
	global_load_dwordx4 v[150:153], v[6:7], off
	v_lshl_add_u64 v[10:11], v[10:11], 0, v[194:195]
	v_lshl_add_u64 v[14:15], v[2:3], 2, v[14:15]
	global_load_dwordx4 v[154:157], v[10:11], off
	v_lshlrev_b64 v[2:3], 8, v[2:3]
	global_load_dword v158, v[14:15], off
	v_lshl_add_u64 v[2:3], s[40:41], 0, v[2:3]
	v_lshlrev_b32_e32 v194, 2, v4
	v_lshl_add_u64 v[2:3], v[2:3], 0, v[194:195]
	global_load_dword v159, v[2:3], off
	v_lshlrev_b32_e32 v5, 7, v5
	v_or_b32_e32 v14, v16, v5
	v_lshlrev_b32_e32 v14, 2, v14
	v_or_b32_e32 v5, v17, v5
	v_lshlrev_b32_e32 v5, 2, v5
	v_lshl_add_u32 v3, v149, 2, 0
	v_add_u32_e32 v3, 0x12c40, v3
	v_mov_b32_e32 v160, v14
	v_mov_b32_e32 v161, v5
	v_mov_b32_e32 v162, v3
.LBB0_982:
	s_or_b64 exec, exec, s[0:1]
	s_and_b64 s[0:1], s[66:67], exec
	s_load_dwordx4 s[40:43], s[76:77], 0x50
	s_cselect_b32 s14, s81, 0x100
	s_lshl_b32 s0, s55, 8
	s_add_i32 s9, s0, 0x4000
	s_lshl_b32 s15, s55, 13
	s_and_b64 s[0:1], s[66:67], exec
	s_cselect_b32 s9, s15, s9
	s_lshl_b32 s34, s39, 7
	s_lshl_b32 s38, s38, 6
	v_lshlrev_b32_e32 v29, 4, v149
	s_waitcnt lgkmcnt(0)
	s_add_u32 s0, s42, s64
	v_and_b32_e32 v30, 48, v29
	s_addc_u32 s1, s43, s65
	s_mul_i32 s15, s28, 0x5000
	v_or_b32_e32 v2, s38, v30
	s_add_u32 s30, s40, s15
	s_mul_hi_u32 s15, s28, 0x5000
	v_lshlrev_b32_e32 v194, 2, v2
	s_addc_u32 s31, s41, s15
	global_load_dwordx4 v[18:21], v194, s[30:31]
	global_load_dwordx4 v[32:35], v194, s[0:1]
	global_load_dwordx4 v[14:17], v194, s[0:1] offset:16
	global_load_dwordx4 v[36:39], v194, s[30:31] offset:16
	v_ashrrev_i32_e32 v31, 2, v149
	v_lshlrev_b32_e32 v2, 1, v31
	v_and_b32_e32 v3, 0xffffffe0, v2
	v_lshrrev_b32_e32 v28, 5, v4
	v_add_u32_e32 v10, 0, v3
	v_and_b32_e32 v12, 6, v2
	global_load_dwordx4 v[2:5], v194, s[0:1] offset:48
	global_load_dwordx4 v[6:9], v194, s[0:1] offset:32
	global_load_dwordx4 v[40:43], v194, s[30:31] offset:48
	global_load_dwordx4 v[44:47], v194, s[30:31] offset:32
	v_and_b32_e32 v11, 16, v149
	v_add3_u32 v10, v10, v11, v12
	v_and_b32_e32 v11, 8, v31
	v_mul_u32_u24_e32 v13, 0x110, v30
	v_add3_u32 v13, v10, v11, v13
	v_cvt_pk_bf16_f32 v10, v246, v195
	ds_write_b16 v13, v10 offset:37200
	v_cvt_pk_bf16_f32 v10, v250, v195
	ds_write_b16 v13, v10 offset:37472
	v_cvt_pk_bf16_f32 v10, v247, v195
	ds_write_b16 v13, v10 offset:37744
	v_cvt_pk_bf16_f32 v10, v251, v195
	ds_write_b16 v13, v10 offset:38016
	v_cvt_pk_bf16_f32 v10, v248, v195
	ds_write_b16 v13, v10 offset:38288
	v_cvt_pk_bf16_f32 v10, v252, v195
	ds_write_b16 v13, v10 offset:38560
	v_cvt_pk_bf16_f32 v10, v249, v195
	ds_write_b16 v13, v10 offset:38832
	v_cvt_pk_bf16_f32 v10, v242, v195
	ds_write_b16 v13, v10 offset:39104
	v_cvt_pk_bf16_f32 v10, v239, v195
	ds_write_b16 v13, v10 offset:39376
	v_cvt_pk_bf16_f32 v10, v243, v195
	ds_write_b16 v13, v10 offset:39648
	v_cvt_pk_bf16_f32 v10, v240, v195
	ds_write_b16 v13, v10 offset:39920
	v_cvt_pk_bf16_f32 v10, v244, v195
	ds_write_b16 v13, v10 offset:40192
	v_cvt_pk_bf16_f32 v10, v241, v195
	v_lshl_add_u64 v[26:27], s[30:31], 0, v[194:195]
	ds_write_b16 v13, v10 offset:40464
	v_add_co_u32_e32 v10, vcc, s81, v26
	v_cvt_pk_bf16_f32 v12, v253, v195
	ds_write_b16 v13, v12 offset:36928
	s_nop 0
	v_addc_co_u32_e32 v11, vcc, 0, v27, vcc
	global_load_dwordx4 v[48:51], v[10:11], off offset:-4096
	global_load_dwordx4 v[52:55], v[10:11], off
	s_waitcnt vmcnt(10)
	v_add_u32_e32 v64, s34, v31
	s_or_b32 s0, s14, 2
	v_cmp_lt_i32_e32 vcc, 1, v64
	v_cmp_gt_u32_e64 s[0:1], s0, v64
	v_cvt_pk_bf16_f32 v10, v238, v195
	s_and_b64 vcc, vcc, s[0:1]
	ds_write_b16 v13, v10 offset:41008
	v_cndmask_b32_e32 v10, 0, v118, vcc
	v_lshlrev_b32_e32 v11, 16, v10
	v_and_b32_e32 v10, 0xffff0000, v10
	s_mov_b64 s[0:1], 0x1000
	v_cvt_pk_bf16_f32 v12, v245, v195
	ds_write_b16 v13, v12 offset:40736
	v_cndmask_b32_e32 v131, 0, v119, vcc
	v_cndmask_b32_e32 v130, 0, v120, vcc
	v_cndmask_b32_e32 v65, 0, v121, vcc
	v_cndmask_b32_e32 v135, 0, v122, vcc
	v_cndmask_b32_e32 v134, 0, v123, vcc
	v_cndmask_b32_e32 v133, 0, v124, vcc
	v_cndmask_b32_e32 v132, 0, v125, vcc
	v_cmp_lt_i32_e32 vcc, 0, v64
	v_lshlrev_b32_e32 v174, 2, v28
	s_waitcnt vmcnt(8)
	v_fma_f32 v136, v18, v11, v32
	v_fma_f32 v137, v19, v10, v33
	v_lshl_add_u64 v[10:11], v[26:27], 0, s[0:1]
	s_mov_b64 s[0:1], 0x2000
	global_load_dwordx4 v[22:25], v[10:11], off offset:32
	global_load_dwordx4 v[56:59], v[10:11], off offset:16
	v_lshl_add_u64 v[32:33], v[26:27], 0, s[0:1]
	global_load_dwordx4 v[10:13], v[10:11], off offset:48
	s_nop 0
	global_load_dwordx4 v[60:63], v[32:33], off offset:16
	v_lshlrev_b32_e32 v18, 16, v131
	v_fma_f32 v34, v20, v18, v34
	v_and_b32_e32 v18, 0xffff0000, v131
	v_fmac_f32_e32 v35, v21, v18
	v_lshlrev_b32_e32 v18, 16, v130
	s_waitcnt vmcnt(10)
	v_fma_f32 v14, v36, v18, v14
	v_and_b32_e32 v18, 0xffff0000, v130
	v_fma_f32 v15, v37, v18, v15
	v_lshlrev_b32_e32 v18, 16, v65
	v_fma_f32 v16, v38, v18, v16
	v_and_b32_e32 v18, 0xffff0000, v65
	v_fmac_f32_e32 v17, v39, v18
	v_lshlrev_b32_e32 v18, 16, v135
	s_waitcnt vmcnt(6)
	v_fma_f32 v44, v44, v18, v6
	global_load_dwordx4 v[18:21], v[32:33], off offset:48
	global_load_dwordx4 v[36:39], v[32:33], off offset:32
	v_and_b32_e32 v6, 0xffff0000, v135
	v_fma_f32 v45, v45, v6, v7
	v_lshlrev_b32_e32 v6, 16, v134
	v_fma_f32 v8, v46, v6, v8
	v_and_b32_e32 v6, 0xffff0000, v134
	v_fmac_f32_e32 v9, v47, v6
	v_lshlrev_b32_e32 v6, 16, v133
	v_fma_f32 v46, v40, v6, v2
	v_and_b32_e32 v2, 0xffff0000, v133
	v_fma_f32 v47, v41, v2, v3
	v_lshlrev_b32_e32 v2, 16, v132
	v_cmp_ge_i32_e64 s[0:1], s14, v64
	v_fma_f32 v4, v42, v2, v4
	v_and_b32_e32 v2, 0xffff0000, v132
	s_and_b64 vcc, vcc, s[0:1]
	v_fmac_f32_e32 v5, v43, v2
	v_cndmask_b32_e32 v32, 0, v69, vcc
	v_cndmask_b32_e32 v33, 0, v68, vcc
	v_cndmask_b32_e32 v40, 0, v67, vcc
	v_cndmask_b32_e32 v41, 0, v66, vcc
	v_cndmask_b32_e32 v65, 0, v73, vcc
	v_cndmask_b32_e32 v130, 0, v72, vcc
	v_cndmask_b32_e32 v42, 0, v71, vcc
	v_cndmask_b32_e32 v43, 0, v70, vcc
	v_cmp_gt_u32_e32 vcc, s14, v64
	v_lshlrev_b32_e32 v2, 16, v41
	s_waitcnt vmcnt(7)
	v_mov_b32_e32 v6, v48
	v_cndmask_b32_e32 v134, 0, v74, vcc
	v_lshlrev_b32_e32 v3, 16, v134
	s_waitcnt vmcnt(6)
	v_mov_b32_e32 v7, v52
	v_pk_mul_f32 v[2:3], v[6:7], v[2:3]
	v_mov_b32_e32 v52, v49
	v_add_f32_e32 v2, v136, v2
	v_add_f32_e32 v48, v2, v3
	v_and_b32_e32 v3, 0xffff0000, v134
	v_and_b32_e32 v2, 0xffff0000, v41
	v_pk_mul_f32 v[2:3], v[52:53], v[2:3]
	v_cndmask_b32_e32 v133, 0, v75, vcc
	v_add_f32_e32 v2, v137, v2
	v_add_f32_e32 v49, v2, v3
	v_lshlrev_b32_e32 v3, 16, v133
	v_lshlrev_b32_e32 v2, 16, v40
	v_mov_b32_e32 v6, v50
	v_mov_b32_e32 v7, v54
	v_pk_mul_f32 v[2:3], v[6:7], v[2:3]
	v_mov_b32_e32 v54, v51
	v_add_f32_e32 v2, v34, v2
	v_add_f32_e32 v50, v2, v3
	v_and_b32_e32 v3, 0xffff0000, v133
	v_and_b32_e32 v2, 0xffff0000, v40
	v_pk_mul_f32 v[2:3], v[54:55], v[2:3]
	v_cndmask_b32_e32 v132, 0, v76, vcc
	v_add_f32_e32 v2, v35, v2
	v_add_f32_e32 v51, v2, v3
	v_lshlrev_b32_e32 v3, 16, v132
	v_lshlrev_b32_e32 v2, 16, v33
	v_cndmask_b32_e32 v131, 0, v77, vcc
	v_cndmask_b32_e32 v140, 0, v78, vcc
	s_movk_i32 s0, 0x4000
	v_cndmask_b32_e32 v135, 0, v81, vcc
	v_cndmask_b32_e32 v138, 0, v80, vcc
	v_cndmask_b32_e32 v139, 0, v79, vcc
	s_waitcnt vmcnt(4)
	v_mov_b32_e32 v6, v56
	s_waitcnt vmcnt(2)
	v_mov_b32_e32 v7, v60
	v_pk_mul_f32 v[2:3], v[6:7], v[2:3]
	v_mov_b32_e32 v60, v57
	v_add_f32_e32 v2, v14, v2
	v_add_f32_e32 v52, v2, v3
	v_and_b32_e32 v3, 0xffff0000, v132
	v_and_b32_e32 v2, 0xffff0000, v33
	v_pk_mul_f32 v[2:3], v[60:61], v[2:3]
	v_mov_b32_e32 v6, v58
	v_add_f32_e32 v2, v15, v2
	v_add_f32_e32 v53, v2, v3
	v_lshlrev_b32_e32 v3, 16, v131
	v_lshlrev_b32_e32 v2, 16, v32
	v_mov_b32_e32 v7, v62
	v_pk_mul_f32 v[2:3], v[6:7], v[2:3]
	v_mov_b32_e32 v62, v59
	v_add_f32_e32 v2, v16, v2
	v_add_f32_e32 v54, v2, v3
	v_and_b32_e32 v3, 0xffff0000, v131
	v_and_b32_e32 v2, 0xffff0000, v32
	v_pk_mul_f32 v[2:3], v[62:63], v[2:3]
	v_mov_b32_e32 v6, v22
	v_add_f32_e32 v2, v17, v2
	v_add_f32_e32 v55, v2, v3
	v_lshlrev_b32_e32 v3, 16, v140
	v_lshlrev_b32_e32 v2, 16, v43
	s_waitcnt vmcnt(0)
	v_mov_b32_e32 v7, v36
	v_pk_mul_f32 v[2:3], v[6:7], v[2:3]
	v_add_co_u32_e32 v6, vcc, s0, v26
	v_add_f32_e32 v2, v44, v2
	s_nop 0
	v_addc_co_u32_e32 v7, vcc, 0, v27, vcc
	global_load_dwordx4 v[14:17], v[6:7], off offset:-4096
	global_load_dwordx4 v[32:35], v[6:7], off
	v_add_f32_e32 v56, v2, v3
	v_and_b32_e32 v3, 0xffff0000, v140
	v_and_b32_e32 v2, 0xffff0000, v43
	v_mov_b32_e32 v36, v23
	v_pk_mul_f32 v[2:3], v[36:37], v[2:3]
	v_mov_b32_e32 v6, v24
	v_add_f32_e32 v2, v45, v2
	v_add_f32_e32 v57, v2, v3
	v_lshlrev_b32_e32 v3, 16, v139
	v_lshlrev_b32_e32 v2, 16, v42
	v_mov_b32_e32 v7, v38
	v_pk_mul_f32 v[2:3], v[6:7], v[2:3]
	v_mov_b32_e32 v38, v25
	v_add_f32_e32 v2, v8, v2
	v_add_f32_e32 v58, v2, v3
	v_and_b32_e32 v3, 0xffff0000, v139
	v_and_b32_e32 v2, 0xffff0000, v42
	v_pk_mul_f32 v[2:3], v[38:39], v[2:3]
	v_lshl_add_u64 v[36:37], v[26:27], 0, s[16:17]
	v_add_f32_e32 v2, v9, v2
	s_mov_b64 s[0:1], 0x4000
	v_add_f32_e32 v59, v2, v3
	v_lshlrev_b32_e32 v3, 16, v138
	v_lshlrev_b32_e32 v2, 16, v130
	global_load_dwordx4 v[6:9], v[36:37], off offset:32
	global_load_dwordx4 v[22:25], v[36:37], off offset:16
	v_lshl_add_u64 v[26:27], v[26:27], 0, s[0:1]
	global_load_dwordx4 v[36:39], v[36:37], off offset:48
	s_nop 0
	global_load_dwordx4 v[40:43], v[26:27], off offset:16
	v_mov_b32_e32 v44, v10
	v_mov_b32_e32 v45, v18
	v_pk_mul_f32 v[2:3], v[44:45], v[2:3]
	v_mov_b32_e32 v18, v11
	v_add_f32_e32 v2, v46, v2
	v_add_f32_e32 v44, v2, v3
	v_and_b32_e32 v3, 0xffff0000, v138
	v_and_b32_e32 v2, 0xffff0000, v130
	v_pk_mul_f32 v[2:3], v[18:19], v[2:3]
	v_mov_b32_e32 v10, v12
	v_add_f32_e32 v2, v47, v2
	v_add_f32_e32 v45, v2, v3
	v_lshlrev_b32_e32 v3, 16, v135
	v_lshlrev_b32_e32 v2, 16, v65
	v_mov_b32_e32 v11, v20
	v_pk_mul_f32 v[2:3], v[10:11], v[2:3]
	v_mov_b32_e32 v20, v13
	v_add_f32_e32 v2, v4, v2
	v_add_f32_e32 v46, v2, v3
	v_and_b32_e32 v3, 0xffff0000, v135
	v_and_b32_e32 v2, 0xffff0000, v65
	v_pk_mul_f32 v[2:3], v[20:21], v[2:3]
	v_add_u32_e32 v18, 1, v64
	v_add_f32_e32 v2, v5, v2
	v_add_f32_e32 v47, v2, v3
	global_load_dwordx4 v[2:5], v[26:27], off offset:48
	global_load_dwordx4 v[10:13], v[26:27], off offset:32
	v_cmp_lt_i32_e32 vcc, -2, v64
	v_cmp_gt_u32_e64 s[0:1], s14, v18
	s_and_b64 vcc, vcc, s[0:1]
	v_add_u32_e32 v18, 2, v64
	v_cndmask_b32_e32 v26, 0, v85, vcc
	v_cndmask_b32_e32 v27, 0, v84, vcc
	v_cndmask_b32_e32 v60, 0, v83, vcc
	v_cndmask_b32_e32 v61, 0, v82, vcc
	v_cndmask_b32_e32 v62, 0, v89, vcc
	v_cndmask_b32_e32 v63, 0, v88, vcc
	v_cndmask_b32_e32 v65, 0, v87, vcc
	v_cndmask_b32_e32 v130, 0, v86, vcc
	v_cmp_lt_i32_e32 vcc, -3, v64
	v_cmp_gt_u32_e64 s[0:1], s14, v18
	s_and_b64 vcc, vcc, s[0:1]
	v_cndmask_b32_e32 v133, 0, v90, vcc
	v_lshlrev_b32_e32 v19, 16, v133
	v_lshlrev_b32_e32 v18, 16, v61
	v_cndmask_b32_e32 v132, 0, v91, vcc
	v_cndmask_b32_e32 v131, 0, v92, vcc
	v_cndmask_b32_e32 v64, 0, v93, vcc
	v_cndmask_b32_e32 v137, 0, v94, vcc
	v_cndmask_b32_e32 v136, 0, v95, vcc
	v_cndmask_b32_e32 v135, 0, v96, vcc
	v_cndmask_b32_e32 v134, 0, v97, vcc
	s_waitcnt vmcnt(7)
	v_mov_b32_e32 v20, v14
	s_waitcnt vmcnt(6)
	v_mov_b32_e32 v21, v32
	v_pk_mul_f32 v[18:19], v[20:21], v[18:19]
	v_mov_b32_e32 v32, v15
	v_add_f32_e32 v14, v48, v18
	v_add_f32_e32 v20, v14, v19
	v_and_b32_e32 v19, 0xffff0000, v133
	v_and_b32_e32 v18, 0xffff0000, v61
	v_pk_mul_f32 v[14:15], v[32:33], v[18:19]
	v_mov_b32_e32 v18, v16
	v_add_f32_e32 v14, v49, v14
	v_add_f32_e32 v21, v14, v15
	v_lshlrev_b32_e32 v15, 16, v132
	v_lshlrev_b32_e32 v14, 16, v60
	v_mov_b32_e32 v19, v34
	v_pk_mul_f32 v[14:15], v[18:19], v[14:15]
	v_mov_b32_e32 v34, v17
	v_add_f32_e32 v14, v50, v14
	v_add_f32_e32 v18, v14, v15
	v_and_b32_e32 v15, 0xffff0000, v132
	v_and_b32_e32 v14, 0xffff0000, v60
	v_pk_mul_f32 v[14:15], v[34:35], v[14:15]
	v_cmp_gt_u32_e64 s[0:1], s18, v149
	v_add_f32_e32 v14, v51, v14
	v_add_f32_e32 v19, v14, v15
	v_lshlrev_b32_e32 v15, 16, v131
	v_lshlrev_b32_e32 v14, 16, v27
	s_waitcnt vmcnt(4)
	v_mov_b32_e32 v16, v22
	s_waitcnt vmcnt(2)
	v_mov_b32_e32 v17, v40
	v_pk_mul_f32 v[14:15], v[16:17], v[14:15]
	v_mov_b32_e32 v40, v23
	v_add_f32_e32 v14, v52, v14
	v_add_f32_e32 v22, v14, v15
	v_and_b32_e32 v15, 0xffff0000, v131
	v_and_b32_e32 v14, 0xffff0000, v27
	v_pk_mul_f32 v[14:15], v[40:41], v[14:15]
	v_mov_b32_e32 v16, v24
	v_add_f32_e32 v14, v53, v14
	v_add_f32_e32 v23, v14, v15
	v_lshlrev_b32_e32 v15, 16, v64
	v_lshlrev_b32_e32 v14, 16, v26
	v_mov_b32_e32 v17, v42
	v_pk_mul_f32 v[14:15], v[16:17], v[14:15]
	v_mov_b32_e32 v42, v25
	v_add_f32_e32 v14, v54, v14
	v_add_f32_e32 v24, v14, v15
	v_and_b32_e32 v15, 0xffff0000, v64
	v_and_b32_e32 v14, 0xffff0000, v26
	v_pk_mul_f32 v[14:15], v[42:43], v[14:15]
	v_mov_b32_e32 v16, v6
	v_add_f32_e32 v14, v55, v14
	v_add_f32_e32 v25, v14, v15
	v_lshlrev_b32_e32 v15, 16, v137
	v_lshlrev_b32_e32 v14, 16, v130
	s_waitcnt vmcnt(0)
	v_mov_b32_e32 v17, v10
	v_pk_mul_f32 v[14:15], v[16:17], v[14:15]
	v_mov_b32_e32 v10, v7
	v_add_f32_e32 v6, v56, v14
	v_add_f32_e32 v16, v6, v15
	v_and_b32_e32 v15, 0xffff0000, v137
	v_and_b32_e32 v14, 0xffff0000, v130
	v_pk_mul_f32 v[6:7], v[10:11], v[14:15]
	v_mov_b32_e32 v10, v8
	v_add_f32_e32 v6, v57, v6
	v_add_f32_e32 v14, v6, v7
	v_lshlrev_b32_e32 v7, 16, v136
	v_lshlrev_b32_e32 v6, 16, v65
	v_mov_b32_e32 v11, v12
	v_pk_mul_f32 v[6:7], v[10:11], v[6:7]
	v_mov_b32_e32 v12, v9
	v_add_f32_e32 v6, v58, v6
	v_add_f32_e32 v10, v6, v7
	v_and_b32_e32 v7, 0xffff0000, v136
	v_and_b32_e32 v6, 0xffff0000, v65
	v_pk_mul_f32 v[6:7], v[12:13], v[6:7]
	v_mov_b32_e32 v8, v36
	v_add_f32_e32 v6, v59, v6
	v_add_f32_e32 v11, v6, v7
	v_lshlrev_b32_e32 v7, 16, v135
	v_lshlrev_b32_e32 v6, 16, v63
	v_mov_b32_e32 v9, v2
	v_pk_mul_f32 v[6:7], v[8:9], v[6:7]
	v_mul_f32_e32 v12, 0xbfb8aa3b, v22
	v_add_f32_e32 v2, v44, v6
	v_add_f32_e32 v8, v2, v7
	v_and_b32_e32 v7, 0xffff0000, v135
	v_and_b32_e32 v6, 0xffff0000, v63
	v_mov_b32_e32 v2, v37
	v_pk_mul_f32 v[2:3], v[2:3], v[6:7]
	v_mov_b32_e32 v6, v38
	v_add_f32_e32 v2, v45, v2
	v_add_f32_e32 v9, v2, v3
	v_lshlrev_b32_e32 v3, 16, v134
	v_lshlrev_b32_e32 v2, 16, v62
	v_mov_b32_e32 v7, v4
	v_pk_mul_f32 v[2:3], v[6:7], v[2:3]
	v_mov_b32_e32 v4, v39
	v_add_f32_e32 v2, v46, v2
	v_add_f32_e32 v6, v2, v3
	v_and_b32_e32 v3, 0xffff0000, v134
	v_and_b32_e32 v2, 0xffff0000, v62
	v_pk_mul_f32 v[2:3], v[4:5], v[2:3]
	v_mul_f32_e32 v4, 0xbfb8aa3b, v20
	v_mul_f32_e32 v5, 0xbfb8aa3b, v21
	v_exp_f32_e32 v4, v4
	v_exp_f32_e32 v5, v5
	v_mul_f32_e32 v7, 0xbfb8aa3b, v18
	v_exp_f32_e32 v7, v7
	v_add_f32_e32 v4, 1.0, v4
	v_add_f32_e32 v5, 1.0, v5
	v_rcp_f32_e32 v4, v4
	v_rcp_f32_e32 v5, v5
	v_add_f32_e32 v2, v47, v2
	v_add_f32_e32 v2, v2, v3
	v_mul_f32_e32 v3, v20, v4
	v_mul_f32_e32 v4, v21, v5
	v_add_f32_e32 v5, 1.0, v7
	v_mul_f32_e32 v7, 0xbfb8aa3b, v19
	v_exp_f32_e32 v7, v7
	v_rcp_f32_e32 v5, v5
	v_mul_f32_e32 v20, 0xbfb8aa3b, v10
	v_exp_f32_e32 v20, v20
	v_add_f32_e32 v7, 1.0, v7
	v_rcp_f32_e32 v7, v7
	v_mul_f32_e32 v5, v18, v5
	v_mul_f32_e32 v18, 0xbfb8aa3b, v16
	v_exp_f32_e32 v18, v18
	v_mul_f32_e32 v7, v19, v7
	v_mul_f32_e32 v19, 0xbfb8aa3b, v14
	v_exp_f32_e32 v19, v19
	v_add_f32_e32 v18, 1.0, v18
	v_add_f32_e32 v20, 1.0, v20
	v_mul_f32_e32 v21, 0xbfb8aa3b, v11
	v_add_f32_e32 v19, 1.0, v19
	v_rcp_f32_e32 v18, v18
	v_rcp_f32_e32 v19, v19
	v_rcp_f32_e32 v20, v20
	v_exp_f32_e32 v21, v21
	v_mul_f32_e32 v16, v16, v18
	v_mul_f32_e32 v14, v14, v19
	v_mul_f32_e32 v10, v10, v20
	v_add_f32_e32 v18, 1.0, v21
	v_mul_f32_e32 v19, 0xbfb8aa3b, v8
	v_mul_f32_e32 v20, 0xbfb8aa3b, v9
	v_rcp_f32_e32 v18, v18
	v_exp_f32_e32 v19, v19
	v_exp_f32_e32 v20, v20
	v_mul_f32_e32 v21, 0xbfb8aa3b, v2
	v_mul_f32_e32 v13, 0xbfb8aa3b, v23
	v_mul_f32_e32 v15, 0xbfb8aa3b, v24
	v_mul_f32_e32 v17, 0xbfb8aa3b, v25
	v_exp_f32_e32 v21, v21
	v_exp_f32_e32 v12, v12
	v_exp_f32_e32 v13, v13
	v_exp_f32_e32 v15, v15
	v_exp_f32_e32 v17, v17
	v_mul_f32_e32 v11, v11, v18
	v_add_f32_e32 v18, 1.0, v19
	v_add_f32_e32 v19, 1.0, v20
	v_mul_f32_e32 v20, 0xbfb8aa3b, v6
	v_exp_f32_e32 v20, v20
	v_add_f32_e32 v21, 1.0, v21
	v_add_f32_e32 v12, 1.0, v12
	v_add_f32_e32 v13, 1.0, v13
	v_add_f32_e32 v15, 1.0, v15
	v_add_f32_e32 v17, 1.0, v17
	v_rcp_f32_e32 v19, v19
	v_rcp_f32_e32 v21, v21
	v_rcp_f32_e32 v12, v12
	v_rcp_f32_e32 v13, v13
	v_rcp_f32_e32 v15, v15
	v_rcp_f32_e32 v17, v17
	v_rcp_f32_e32 v18, v18
	v_add_f32_e32 v20, 1.0, v20
	v_rcp_f32_e32 v20, v20
	v_mul_f32_e32 v9, v9, v19
	v_mul_f32_e32 v19, v2, v21
	v_cvt_pk_bf16_f32 v2, v3, v4
	v_cvt_pk_bf16_f32 v3, v5, v7
	v_cvt_pk_bf16_f32 v7, v10, v11
	v_mul_lo_u32 v10, v31, s21
	v_lshlrev_b32_e32 v11, 1, v30
	v_mul_f32_e32 v12, v22, v12
	v_mul_f32_e32 v13, v23, v13
	v_mul_f32_e32 v15, v24, v15
	v_mul_f32_e32 v17, v25, v17
	v_mul_f32_e32 v8, v8, v18
	v_cvt_pk_bf16_f32 v4, v12, v13
	v_cvt_pk_bf16_f32 v5, v15, v17
	v_add3_u32 v10, 0, v10, v11
	v_mul_f32_e32 v18, v6, v20
	v_cvt_pk_bf16_f32 v6, v16, v14
	v_cvt_pk_bf16_f32 v8, v8, v9
	v_cvt_pk_bf16_f32 v9, v18, v19
	ds_write_b128 v10, v[2:5] offset:64
	ds_write_b128 v10, v[6:9] offset:80
	ds_write_b128 v10, v[102:105] offset:18496
	ds_write_b128 v10, v[98:101] offset:18512
	v_lshrrev_b32_e32 v2, 3, v149
	v_mul_lo_u32 v2, v2, s21
	v_and_b32_e32 v3, 0x70, v29
	v_add3_u32 v2, 0, v2, v3
	v_cmp_gt_u32_e32 vcc, 0x80, v0
	s_and_saveexec_b64 s[30:31], vcc
	s_cbranch_execz .Lsc_gq_done
	v_readlane_b32 s15, v254, 53
	v_readlane_b32 s14, v254, 47
	v_readlane_b32 s40, v254, 54
	s_waitcnt vmcnt(0)
	v_add_u32_e32 v163, s15, v160
	v_add_f32_e32 v152, v150, v152
	v_add_f32_e32 v157, v150, v158
	v_max_f32_e32 v152, v157, v152
	v_sub_f32_e32 v150, v150, v152
	v_mul_f32_e32 v150, 0x3fb8aa3b, v150
	ds_write_b32 v163, v150
	v_mul_f32_e32 v150, 0x3fb8aa3b, v151
	v_add_u32_e32 v151, 0x12040, v160
	ds_write_b32 v151, v150
	v_sub_f32_e32 v150, v157, v152
	v_mul_f32_e32 v150, 0x3fb8aa3b, v150
	v_exp_f32_e32 v150, v150
	v_add_u32_e32 v151, s14, v160
	ds_write_b32 v151, v150
	v_mul_f32_e32 v150, 0xbfb8aa3b, v152
	v_exp_f32_e32 v150, v150
	v_add_u32_e32 v151, s40, v160
	ds_write_b32 v151, v150
	v_add_f32_e32 v150, v154, v158
	v_add_f32_e32 v151, v154, v156
	v_max_f32_e32 v151, v150, v151
	v_sub_f32_e32 v150, v150, v151
	v_mul_f32_e32 v150, 0x3fb8aa3b, v150
	v_sub_f32_e32 v152, v154, v151
	v_exp_f32_e32 v150, v150
	v_mul_f32_e32 v152, 0x3fb8aa3b, v152
	v_add_u32_e32 v158, s15, v161
	ds_write_b32 v158, v152
	v_mul_f32_e32 v152, 0x3fb8aa3b, v155
	v_add_u32_e32 v158, 0x12040, v161
	ds_write_b32 v158, v152
	v_add_u32_e32 v152, s14, v161
	ds_write_b32 v152, v150
	v_mul_f32_e32 v150, 0xbfb8aa3b, v151
	v_exp_f32_e32 v150, v150
	v_add_u32_e32 v161, s40, v161
	ds_write_b32 v161, v150
	ds_write_b32 v162, v159
.Lsc_gq_done:
	s_or_b64 exec, exec, s[30:31]
	v_cmp_lt_u32_e32 vcc, s80, v149
	ds_write_b128 v2, v[126:129] offset:54336
	ds_write_b128 v2, v[106:109] offset:63552
	s_waitcnt lgkmcnt(0)
	s_barrier
	s_and_saveexec_b64 s[14:15], vcc
	s_xor_b64 s[14:15], exec, s[14:15]
	v_lshlrev_b32_e32 v174, 2, v28
	s_or_saveexec_b64 s[30:31], s[14:15]
	v_and_b32_e32 v50, 31, v149
	v_bfe_u32 v2, v149, 6, 2
	s_add_i32 s9, s9, s34
	v_lshl_or_b32 v150, v2, 5, v50
	v_mov_b32_e32 v51, 3
	v_or_b32_e32 v178, s9, v150
	s_xor_b64 exec, exec, s[30:31]
	s_cbranch_execz .LBB0_986
	s_load_dwordx2 s[14:15], s[76:77], 0x148
	s_lshl_b32 s70, s38, 1
	v_lshlrev_b32_e32 v194, 3, v28
	v_mov_b32_e32 v51, v2
	v_mov_b32_e32 v2, 0
	s_waitcnt lgkmcnt(0)
	v_mov_b64_e32 v[4:5], s[14:15]
	v_mad_i64_i32 v[4:5], s[14:15], v178, s2, v[4:5]
	v_lshl_add_u64 v[4:5], v[4:5], 0, s[70:71]
	v_lshl_add_u64 v[4:5], v[4:5], 0, v[194:195]
	global_load_dwordx2 v[180:181], v[4:5], off offset:3072
	global_load_dwordx2 v[176:177], v[4:5], off offset:3088
	global_load_dwordx2 v[172:173], v[4:5], off offset:3104
	global_load_dwordx2 v[170:171], v[4:5], off offset:3120
	global_load_dwordx2 v[168:169], v[4:5], off offset:3136
	global_load_dwordx2 v[166:167], v[4:5], off offset:3152
	global_load_dwordx2 v[164:165], v[4:5], off offset:3168
	global_load_dwordx2 v[162:163], v[4:5], off offset:3184
